# speedup vs baseline: 1.0767x; 1.0152x over previous
_Z11attn_kernelPKDF16_S0_S0_PDF16_P15HIP_vector_typeIfLj2EE:
	s_mov_b32 s28, s2
	s_load_dwordx4 s[32:35], s[0:1], 0x8
	v_readfirstlane_b32 s3, v0
	s_ashr_i32 s12, s2, 5
	s_lshr_b32 s21, s3, 6
	s_and_b32 s3, s2, 7
	s_and_b32 s12, s12, -8
	s_load_dwordx8 s[4:11], s[0:1], 0x0
	s_or_b32 s12, s12, s3
	s_bfe_u32 s20, s2, 0x10003
	s_lshl_b32 s2, s2, 3
	s_and_b32 s2, s2, 0x780
	s_lshl_b32 s3, s21, 5
	s_ashr_i32 s13, s12, 31
	s_add_i32 s2, s3, s2
	s_lshl_b64 s[16:17], s[12:13], 11
	s_lshl_b32 s3, s20, 10
	s_or_b32 s14, s16, s3
	s_mov_b32 s15, s17
	s_lshl_b64 s[18:19], s[14:15], 7
	s_lshl_b64 s[14:15], s[12:13], 18
	s_waitcnt lgkmcnt(0)
	s_add_u32 s3, s8, s14
	s_addc_u32 s22, s9, s15
	s_add_u32 s16, s16, s2
	v_and_b32_e32 v98, 31, v0
	s_addc_u32 s17, s17, 0
	v_or_b32_e32 v2, s16, v98
	v_mov_b32_e32 v3, s17
	v_bfe_u32 v54, v0, 5, 1
	v_lshlrev_b64 v[2:3], 7, v[2:3]
	v_mov_b32_e32 v51, 0
	v_lshl_add_u64 v[2:3], s[4:5], 0, v[2:3]
	v_lshlrev_b32_e32 v50, 4, v54
	v_lshl_add_u64 v[2:3], v[2:3], 0, v[50:51]
	s_add_u32 s18, s6, s18
	v_bfe_u32 v1, v0, 3, 3
	global_load_dwordx4 v[94:97], v[2:3], off nt
	global_load_dwordx4 v[90:93], v[2:3], off offset:32 nt
	global_load_dwordx4 v[86:89], v[2:3], off offset:64 nt
	global_load_dwordx4 v[82:85], v[2:3], off offset:96 nt
	s_addc_u32 s19, s7, s19
	s_lshl_b32 s24, s20, 11
	v_lshl_or_b32 v2, s21, 4, v1
	v_and_b32_e32 v99, 63, v0
	s_add_u32 s4, s3, s24
	v_or_b32_e32 v3, 8, v2
	v_lshlrev_b32_e32 v4, 4, v0
	s_movk_i32 s3, 0x70
	v_bitop3_b32 v53, v99, s3, v4 bitop3:0x48
	v_lshrrev_b32_e32 v4, 1, v3
	v_xor_b32_e32 v4, v4, v0
	s_addc_u32 s5, s22, 0
	v_lshlrev_b32_e32 v4, 4, v4
	s_lshl_b32 s22, s21, 11
	v_and_b32_e32 v52, 0x70, v4
	v_lshl_or_b32 v55, v2, 7, v53
	s_mov_b32 m0, s22
	v_lshl_or_b32 v64, v3, 7, v52
	global_load_lds_dwordx4 v55, s[18:19]
	s_or_b32 m0, s22, 0x400
	v_lshl_or_b32 v50, v2, 12, v53
	global_load_lds_dwordx4 v64, s[18:19]
	s_add_i32 m0, s22, 0x2000
	v_lshl_or_b32 v2, v3, 12, v52
	global_load_lds_dwordx4 v50, s[4:5]
	s_add_i32 m0, s22, 0x2400
	v_mov_b32_e32 v3, v51
	global_load_lds_dwordx4 v2, s[4:5]
	s_add_i32 m0, s22, 0x4000
	v_lshl_add_u64 v[60:61], s[4:5], 0, v[50:51]
	v_lshl_add_u64 v[62:63], s[4:5], 0, v[2:3]
	s_add_u32 s4, s18, 0x2000
	s_addc_u32 s5, s19, 0
	global_load_lds_dwordx4 v55, s[4:5]
	s_add_i32 m0, s22, 0x4400
	s_load_dwordx2 s[0:1], s[0:1], 0x20
	global_load_lds_dwordx4 v64, s[4:5]
	s_mov_b64 s[4:5], 0x80
	v_lshl_add_u64 v[2:3], v[60:61], 0, s[4:5]
	s_add_i32 m0, s22, 0x6000
	v_lshrrev_b32_e32 v4, 1, v0
	global_load_lds_dwordx4 v[2:3], off
	v_lshl_add_u64 v[2:3], v[62:63], 0, s[4:5]
	s_add_i32 m0, s22, 0x6400
	v_and_b32_e32 v5, 4, v4
	global_load_lds_dwordx4 v[2:3], off
	v_lshlrev_b32_e32 v3, 1, v0
	v_and_b32_e32 v2, 19, v0
	v_and_b32_e32 v3, 8, v3
	v_or3_b32 v2, v3, v2, v5
	s_waitcnt vmcnt(4)
	v_lshlrev_b32_e32 v115, 7, v2
	v_lshrrev_b32_e32 v3, 1, v2
	v_bfe_u32 v46, v2, 1, 3
	v_bitop3_b32 v2, v54, v4, 7 bitop3:0x78
	s_mov_b32 s3, 0
	v_lshlrev_b32_e32 v108, 3, v54
	s_mov_b32 s23, 1
	s_mov_b64 s[16:17], 0x2000
	v_lshlrev_b32_e32 v109, 7, v98
	v_lshlrev_b32_e32 v110, 4, v2
	s_movk_i32 s25, 0x400
	v_bfe_u32 v50, v0, 1, 3
	s_barrier
	v_bitop3_b32 v2, v54, v3, 7 bitop3:0x78
	v_lshlrev_b32_e32 v116, 4, v2
	v_or_b32_e32 v6, v115, v116
	ds_read_b128 v[2:5], v6
	ds_read_b128 v[18:21], v6 offset:4096
	v_bitop3_b32 v6, v54, v46, 2 bitop3:0x36
	v_lshlrev_b32_e32 v117, 4, v6
	v_or_b32_e32 v6, v115, v117
	ds_read_b128 v[34:37], v6
	ds_read_b128 v[38:41], v6 offset:4096
	s_waitcnt vmcnt(4) lgkmcnt(0)
	v_mfma_f32_32x32x16_f16 v[2:17], v[2:5], v[94:97], 0
	v_bitop3_b32 v42, v54, v46, 4 bitop3:0x36
	v_bitop3_b32 v46, v54, v46, 6 bitop3:0x36
	v_lshlrev_b32_e32 v118, 4, v42
	v_lshlrev_b32_e32 v119, 4, v46
	v_or_b32_e32 v42, v115, v118
	v_or_b32_e32 v56, v115, v119
	v_mfma_f32_32x32x16_f16 v[18:33], v[18:21], v[94:97], 0
	v_mfma_f32_32x32x16_f16 v[2:17], v[34:37], v[90:93], v[2:17]
	ds_read_b128 v[34:37], v42
	ds_read_b128 v[42:45], v42 offset:4096
	ds_read_b128 v[46:49], v56
	ds_read_b128 v[56:59], v56 offset:4096
	v_mfma_f32_32x32x16_f16 v[18:33], v[38:41], v[90:93], v[18:33]
	s_waitcnt lgkmcnt(3)
	v_mfma_f32_32x32x16_f16 v[2:17], v[34:37], v[86:89], v[2:17]
	s_waitcnt lgkmcnt(2)
	v_mfma_f32_32x32x16_f16 v[18:33], v[42:45], v[86:89], v[18:33]
	s_waitcnt lgkmcnt(1)
	v_mfma_f32_32x32x16_f16 v[2:17], v[46:49], v[82:85], v[2:17]
	s_waitcnt lgkmcnt(0)
	v_mfma_f32_32x32x16_f16 v[18:33], v[56:59], v[82:85], v[18:33]
	s_add_i32 m0, s22, 0x8000
	s_add_u32 s18, s18, 0x4000
	s_addc_u32 s19, s19, 0
	global_load_lds_dwordx4 v55, s[18:19]
	s_add_i32 m0, s22, 0x8400
	s_nop 0
	global_load_lds_dwordx4 v64, s[18:19]
	s_mov_b64 s[18:19], 0x100
	v_lshl_add_u64 v[34:35], v[60:61], 0, s[18:19]
	s_add_i32 m0, s22, 0xa000
	s_nop 0
	global_load_lds_dwordx4 v[34:35], off
	v_lshl_add_u64 v[34:35], v[62:63], 0, s[18:19]
	s_add_i32 m0, s22, 0xa400
	s_mov_b32 s18, 0x8000
	global_load_lds_dwordx4 v[34:35], off
	v_max3_f32 v34, v2, v3, v4
	v_max3_f32 v34, v34, v5, v6
	v_max3_f32 v34, v34, v7, v8
	v_max3_f32 v34, v34, v9, v10
	v_max3_f32 v34, v34, v11, v12
	v_max3_f32 v34, v34, v13, v14
	v_max3_f32 v34, v34, v15, v16
	v_max_f32 v34, v34, v17
	v_max3_f32 v35, v18, v19, v20
	v_max3_f32 v35, v35, v21, v22
	v_max3_f32 v35, v35, v23, v24
	v_max3_f32 v35, v35, v25, v26
	v_max3_f32 v35, v35, v27, v28
	v_max3_f32 v35, v35, v29, v30
	v_max3_f32 v35, v35, v31, v32
	v_max_f32 v35, v35, v33
	s_nop 0
	v_max3_f32 v34, v34, v35, v35
	s_nop 0
	v_mov_b32_e32 v35, v34
	s_nop 1
	v_permlane32_swap_b32_e32 v34, v35
	v_max3_f32 v47, v34, v35, v35
	s_nop 0
	v_sub_f32_e32 v10, v10, v47
	v_exp_f32_e32 v126, v10
	v_bitop3_b32 v10, v54, v50, 2 bitop3:0x36
	v_sub_f32_e32 v6, v6, v47
	v_lshlrev_b32_e32 v112, 4, v10
	v_sub_f32_e32 v2, v2, v47
	v_sub_f32_e32 v3, v3, v47
	v_sub_f32_e32 v4, v4, v47
	v_sub_f32_e32 v5, v5, v47
	v_sub_f32_e32 v7, v7, v47
	v_sub_f32_e32 v8, v8, v47
	v_sub_f32_e32 v9, v9, v47
	v_exp_f32_e32 v106, v6
	v_or_b32_e32 v6, v109, v110
	v_or_b32_e32 v10, v109, v112
	v_sub_f32_e32 v19, v19, v47
	v_sub_f32_e32 v20, v20, v47
	v_sub_f32_e32 v21, v21, v47
	v_sub_f32_e32 v22, v22, v47
	v_exp_f32_e32 v80, v2
	v_exp_f32_e32 v100, v3
	v_exp_f32_e32 v102, v4
	v_exp_f32_e32 v104, v5
	v_exp_f32_e32 v120, v7
	v_exp_f32_e32 v122, v8
	v_exp_f32_e32 v124, v9
	ds_read_b128 v[2:5], v6 offset:8192
	ds_read_b128 v[6:9], v6 offset:12288
	ds_read_b128 v[56:59], v10 offset:8192
	ds_read_b128 v[60:63], v10 offset:12288
	v_exp_f32_e32 v101, v19
	v_exp_f32_e32 v103, v20
	v_exp_f32_e32 v105, v21
	v_exp_f32_e32 v107, v22
	v_sub_f32_e32 v34, 0, v47
	v_mov_b32_e32 v35, v34
	v_mov_b32_e32 v36, v34
	v_mov_b32_e32 v37, v34
	v_mov_b32_e32 v38, v34
	v_mov_b32_e32 v39, v34
	v_mov_b32_e32 v40, v34
	v_mov_b32_e32 v41, v34
	v_mov_b32_e32 v42, v34
	v_mov_b32_e32 v43, v34
	v_mov_b32_e32 v44, v34
	v_mov_b32_e32 v45, v34
	v_mov_b32_e32 v46, v34
	v_sub_f32_e32 v18, v18, v47
	v_sub_f32_e32 v23, v23, v47
	v_sub_f32_e32 v24, v24, v47
	v_sub_f32_e32 v25, v25, v47
	v_sub_f32_e32 v26, v26, v47
	v_sub_f32_e32 v27, v27, v47
	v_sub_f32_e32 v28, v28, v47
	v_sub_f32_e32 v29, v29, v47
	v_sub_f32_e32 v30, v30, v47
	v_sub_f32_e32 v31, v31, v47
	v_sub_f32_e32 v32, v32, v47
	v_sub_f32_e32 v33, v33, v47
	v_sub_f32_e32 v11, v11, v47
	v_sub_f32_e32 v12, v12, v47
	v_sub_f32_e32 v13, v13, v47
	v_sub_f32_e32 v14, v14, v47
	v_sub_f32_e32 v15, v15, v47
	v_sub_f32_e32 v16, v16, v47
	v_sub_f32_e32 v17, v17, v47
	v_mov_b32_e32 v47, v34
	v_mov_b32_e32 v48, v34
	v_mov_b32_e32 v49, v34
	v_exp_f32_e32 v128, v11
	v_exp_f32_e32 v130, v12
	v_exp_f32_e32 v132, v13
	v_exp_f32_e32 v134, v14
	v_exp_f32_e32 v136, v15
	v_exp_f32_e32 v138, v16
	v_exp_f32_e32 v140, v17
	v_exp_f32_e32 v81, v18
	v_exp_f32_e32 v121, v23
	v_exp_f32_e32 v123, v24
	v_exp_f32_e32 v125, v25
	v_exp_f32_e32 v127, v26
	v_exp_f32_e32 v129, v27
	v_exp_f32_e32 v131, v28
	v_exp_f32_e32 v133, v29
	v_exp_f32_e32 v135, v30
	v_exp_f32_e32 v137, v31
	v_exp_f32_e32 v139, v32
	v_exp_f32_e32 v141, v33
	v_cvt_pk_f16_f32 v13, v122, v124
	v_cvt_pk_f16_f32 v12, v106, v120
	v_cvt_pk_f16_f32 v11, v102, v104
	v_cvt_pk_f16_f32 v10, v80, v100
	v_cvt_pk_f16_f32 v67, v138, v140
	v_cvt_pk_f16_f32 v66, v134, v136
	s_waitcnt lgkmcnt(0)
	v_mfma_f32_32x32x16_f16 v[18:33], v[2:5], v[10:13], 0
	v_cvt_pk_f16_f32 v65, v130, v132
	v_cvt_pk_f16_f32 v64, v126, v128
	v_bitop3_b32 v55, v54, v50, 4 bitop3:0x36
	v_bitop3_b32 v50, v54, v50, 6 bitop3:0x36
	v_lshlrev_b32_e32 v111, 4, v55
	v_lshlrev_b32_e32 v113, 4, v50
	v_or_b32_e32 v55, v109, v111
	v_mfma_f32_32x32x16_f16 v[2:17], v[6:9], v[10:13], 0
	v_or_b32_e32 v50, v109, v113
	v_mfma_f32_32x32x16_f16 v[18:33], v[56:59], v[64:67], v[18:33]
	ds_read_b128 v[56:59], v55 offset:8192
	ds_read_b128 v[68:71], v55 offset:12288
	ds_read_b128 v[72:75], v50 offset:8192
	ds_read_b128 v[76:79], v50 offset:12288
	v_mfma_f32_32x32x16_f16 v[2:17], v[60:63], v[64:67], v[2:17]
	v_add_f32_e64 v54, v80, 0
	v_add_f32_e64 v55, v81, 0
	v_cvt_pk_f16_f32 v63, v123, v125
	v_add_f32_e64 v54, v54, v100
	v_add_f32_e64 v55, v55, v101
	v_cvt_pk_f16_f32 v62, v107, v121
	v_add_f32_e32 v54, v54, v102
	v_add_f32_e32 v55, v55, v103
	v_cvt_pk_f16_f32 v61, v103, v105
	v_add_f32_e32 v54, v54, v104
	v_add_f32_e32 v55, v55, v105
	v_cvt_pk_f16_f32 v60, v81, v101
	v_add_f32_e32 v54, v54, v106
	v_add_f32_e32 v55, v55, v107
	v_cvt_pk_f16_f32 v67, v139, v141
	v_add_f32_e32 v54, v54, v120
	v_add_f32_e32 v55, v55, v121
	s_waitcnt lgkmcnt(0)
	v_mfma_f32_32x32x16_f16 v[18:33], v[56:59], v[60:63], v[18:33]
	v_add_f32_e64 v54, v54, v122
	v_add_f32_e64 v55, v55, v123
	v_cvt_pk_f16_f32 v66, v135, v137
	v_add_f32_e64 v54, v54, v124
	v_add_f32_e64 v55, v55, v125
	v_cvt_pk_f16_f32 v65, v131, v133
	v_add_f32_e32 v54, v54, v126
	v_add_f32_e32 v55, v55, v127
	v_cvt_pk_f16_f32 v64, v127, v129
	v_add_f32_e32 v54, v54, v128
	v_add_f32_e32 v55, v55, v129
	v_mfma_f32_32x32x16_f16 v[2:17], v[68:71], v[60:63], v[2:17]
	v_add_f32_e64 v54, v54, v130
	v_add_f32_e64 v55, v55, v131
	s_add_u32 s8, s8, s24
	v_add_f32_e64 v54, v54, v132
	v_add_f32_e64 v55, v55, v133
	s_addc_u32 s9, s9, 0
	v_add_f32_e32 v54, v54, v134
	v_add_f32_e32 v55, v55, v135
	s_mov_b64 s[26:27], 0x180
	v_add_f32_e32 v54, v54, v136
	v_add_f32_e32 v55, v55, v137
	v_mfma_f32_32x32x16_f16 v[18:33], v[72:75], v[64:67], v[18:33]
	v_add_f32_e64 v54, v54, v138
	v_add_f32_e64 v55, v55, v139
	v_add_f32_e64 v54, v54, v140
	v_add_f32_e64 v55, v55, v141
	v_add_f32_e32 v50, v54, v55
	v_add_f32_e32 v114, 0, v50
	v_lshlrev_b32_e32 v50, 12, v1
	v_lshl_or_b32 v56, s21, 16, v50
	v_mfma_f32_32x32x16_f16 v[2:17], v[76:79], v[64:67], v[2:17]
	v_or_b32_e32 v50, v56, v53
	v_lshl_add_u64 v[54:55], s[8:9], 0, v[50:51]
	v_or3_b32 v50, v56, v52, s18
	v_lshl_add_u64 v[100:101], v[54:55], 0, s[26:27]
	v_lshl_add_u64 v[54:55], s[8:9], 0, v[50:51]
	s_lshl_b32 s8, s20, 17
	v_lshl_or_b32 v56, v1, 7, s22
	s_add_u32 s6, s6, s8
	v_or_b32_e32 v50, v56, v53
	s_addc_u32 s7, s7, 0
	v_lshl_add_u64 v[102:103], v[54:55], 0, s[26:27]
	v_lshl_add_u64 v[54:55], s[6:7], 0, v[50:51]
	v_or3_b32 v50, v56, v52, s25
	s_mov_b64 s[8:9], 0x6000
	v_lshl_add_u64 v[50:51], s[6:7], 0, v[50:51]
	v_lshl_add_u64 v[104:105], v[54:55], 0, s[8:9]
	v_lshl_add_u64 v[106:107], v[50:51], 0, s[8:9]
	s_mov_b32 s8, 0x46000000
	s_mov_b32 s9, 1
	s_and_b32 s29, s28, 7
	s_lshr_b32 s40, s28, 3
	s_lshr_b32 s41, s40, 5
	s_lshl_b32 s41, s41, 3
	s_or_b32 s29, s41, s29
	s_and_b32 s40, s40, 1
	s_lshl_b32 s29, s29, 18
	s_lshl_b32 s41, s40, 17
	s_lshl_b32 s42, s40, 11
	s_add_i32 s41, s41, s29
	s_add_i32 s41, s41, 0x6000
	s_add_i32 s42, s42, s29
	s_add_i32 s42, s42, 0x180
	v_and_b32_e32 v145, 63, v0
	v_lshrrev_b32_e32 v146, 3, v145
	v_lshl_add_u32 v146, s21, 4, v146
	v_and_b32_e32 v145, 7, v145
	v_bfe_u32 v147, v146, 1, 3
	v_xor_b32_e32 v148, v145, v147
	v_xor_b32_e32 v147, 4, v148
	v_lshlrev_b32_e32 v148, 4, v148
	v_lshlrev_b32_e32 v147, 4, v147
	v_lshl_add_u32 v145, v146, 7, v148
	v_lshl_add_u32 v149, v146, 7, v147
	v_add_u32_e32 v149, 0x400, v149
	v_lshl_add_u32 v148, v146, 12, v148
	v_lshl_add_u32 v147, v146, 12, v147
	v_add_u32_e32 v147, 0x8000, v147
	s_waitcnt lgkmcnt(0)
	s_add_u32 s36, s32, s41
	s_addc_u32 s37, s33, 0
	s_add_u32 s38, s34, s42
	s_addc_u32 s39, s35, 0

.LBB3_5:
.LBB3_6:
	v_add_u32_e32 v167, s18, v109
	v_add_u32_e32 v166, v167, v110
	ds_read_b128 v[158:161], v166 offset:8192
	ds_read_b128 v[162:165], v166 offset:12288
	s_nop 0
	v_exp_f32_e32 v120, v66
	v_exp_f32_e32 v121, v67
	v_exp_f32_e32 v122, v68
	v_exp_f32_e32 v123, v69
	v_exp_f32_e32 v124, v70
	v_exp_f32_e32 v125, v71
	v_exp_f32_e32 v126, v72
	v_exp_f32_e32 v127, v73
	v_exp_f32_e32 v128, v74
	v_exp_f32_e32 v129, v75
	v_exp_f32_e32 v130, v76
	v_exp_f32_e32 v131, v77
	v_exp_f32_e32 v132, v78
	v_exp_f32_e32 v133, v79
	v_exp_f32_e32 v134, v80
	v_exp_f32_e32 v135, v81
	v_exp_f32_e32 v136, v50
	v_exp_f32_e32 v137, v51
	v_exp_f32_e32 v138, v52
	v_exp_f32_e32 v139, v53
	v_exp_f32_e32 v140, v54
	v_exp_f32_e32 v141, v55
	v_exp_f32_e32 v142, v56
	v_exp_f32_e32 v143, v57
	v_exp_f32_e32 v150, v58
	v_exp_f32_e32 v151, v59
	v_exp_f32_e32 v152, v60
	v_exp_f32_e32 v153, v61
	v_exp_f32_e32 v154, v62
	v_exp_f32_e32 v155, v63
	v_exp_f32_e32 v156, v64
	v_exp_f32_e32 v157, v65
	v_add_f32_e32 v144, v120, v121
	v_add_f32_e32 v166, v122, v123
	v_add_f32_e32 v144, v144, v124
	v_add_f32_e32 v166, v166, v125
	v_add_f32_e32 v144, v144, v126
	v_add_f32_e32 v166, v166, v127
	v_add_f32_e32 v144, v144, v128
	v_add_f32_e32 v166, v166, v129
	v_add_f32_e32 v144, v144, v130
	v_add_f32_e32 v166, v166, v131
	v_add_f32_e32 v144, v144, v132
	v_add_f32_e32 v166, v166, v133
	v_add_f32_e32 v144, v144, v134
	v_add_f32_e32 v166, v166, v135
	v_add_f32_e32 v144, v144, v136
	v_add_f32_e32 v166, v166, v137
	v_add_f32_e32 v144, v144, v138
	v_add_f32_e32 v166, v166, v139
	v_add_f32_e32 v144, v144, v140
	v_add_f32_e32 v166, v166, v141
	v_add_f32_e32 v144, v144, v142
	v_add_f32_e32 v166, v166, v143
	v_add_f32_e32 v144, v144, v150
	v_add_f32_e32 v166, v166, v151
	v_add_f32_e32 v144, v144, v152
	v_add_f32_e32 v166, v166, v153
	v_add_f32_e32 v144, v144, v154
	v_add_f32_e32 v166, v166, v155
	v_add_f32_e32 v144, v144, v156
	v_add_f32_e32 v166, v166, v157
	v_add_f32_e32 v144, v144, v166
	s_nop 0
	v_cmp_lt_f32_e32 vcc, s8, v144
	s_cbranch_vccnz .Lattn_slow
	v_add_u32_e32 v166, v167, v112
	ds_read_b128 v[50:53], v166 offset:8192
	ds_read_b128 v[54:57], v166 offset:12288
	s_add_i32 s9, s9, 1
	s_add_i32 s6, s23, 1
	s_cmp_lg_u32 s23, 2
	s_cselect_b32 s23, s6, 0
	v_cvt_pk_f16_f32 v66, v120, v121
	v_cvt_pk_f16_f32 v67, v122, v123
	v_cvt_pk_f16_f32 v68, v124, v125
	v_cvt_pk_f16_f32 v69, v126, v127
	v_cvt_pk_f16_f32 v70, v128, v129
	v_cvt_pk_f16_f32 v71, v130, v131
	v_cvt_pk_f16_f32 v72, v132, v133
	v_cvt_pk_f16_f32 v73, v134, v135
	v_add_u32_e32 v166, v167, v111
	v_add_u32_e32 v167, v167, v113
	s_waitcnt lgkmcnt(2)
	s_setprio 1
	v_mfma_f32_32x32x16_f16 v[18:33], v[158:161], v[66:69], v[18:33]
	v_mfma_f32_32x32x16_f16 v[2:17], v[162:165], v[66:69], v[2:17]
	ds_read_b128 v[58:61], v166 offset:8192
	ds_read_b128 v[62:65], v166 offset:12288
	v_cvt_pk_f16_f32 v74, v136, v137
	v_cvt_pk_f16_f32 v75, v138, v139
	v_cvt_pk_f16_f32 v76, v140, v141
	v_cvt_pk_f16_f32 v77, v142, v143
	s_waitcnt lgkmcnt(2)
	v_mfma_f32_32x32x16_f16 v[18:33], v[50:53], v[70:73], v[18:33]
	v_mfma_f32_32x32x16_f16 v[2:17], v[54:57], v[70:73], v[2:17]
	ds_read_b128 v[120:123], v167 offset:8192
	ds_read_b128 v[124:127], v167 offset:12288
	v_cvt_pk_f16_f32 v78, v150, v151
	v_cvt_pk_f16_f32 v79, v152, v153
	v_cvt_pk_f16_f32 v80, v154, v155
	v_cvt_pk_f16_f32 v81, v156, v157
	v_add_f32_e32 v114, v114, v144
	s_waitcnt lgkmcnt(2)
	v_mfma_f32_32x32x16_f16 v[18:33], v[58:61], v[74:77], v[18:33]
	v_mfma_f32_32x32x16_f16 v[2:17], v[62:65], v[74:77], v[2:17]
	s_waitcnt lgkmcnt(0)
	v_mfma_f32_32x32x16_f16 v[18:33], v[120:123], v[78:81], v[18:33]
	v_mfma_f32_32x32x16_f16 v[2:17], v[124:127], v[78:81], v[2:17]
	s_setprio 0
	s_cmp_eq_u32 s9, 15
	s_cbranch_scc0 .LBB3_1
	s_branch .LBB3_8
.Lattn_slow:
	v_max3_f32 v120, v66, v67, v68
	v_max3_f32 v120, v120, v69, v70
	v_max3_f32 v120, v120, v71, v72
	v_max3_f32 v120, v120, v73, v74
	v_max3_f32 v120, v120, v75, v76
	v_max3_f32 v120, v120, v77, v78
	v_max3_f32 v120, v120, v79, v80
	v_max_f32 v120, v120, v81
	v_max3_f32 v121, v50, v51, v52
	v_max3_f32 v121, v121, v53, v54
	v_max3_f32 v121, v121, v55, v56
	v_max3_f32 v121, v121, v57, v58
	v_max3_f32 v121, v121, v59, v60
	v_max3_f32 v121, v121, v61, v62
	v_max3_f32 v121, v121, v63, v64
	v_max_f32 v121, v121, v65
	s_nop 0
	v_max3_f32 v120, v120, v121, v121
	s_nop 0
	v_mov_b32_e32 v121, v120
	s_nop 1
	v_permlane32_swap_b32_e32 v120, v121
	v_max3_f32 v120, v120, v121, v121
	s_nop 0
.LBB3_7:
	v_max_f32_e32 v120, v120, v120
	v_max_f32_e32 v121, 0, v120
	v_exp_f32_e64 v120, -v121
	v_sub_f32_e32 v66, v66, v121
	v_sub_f32_e32 v67, v67, v121
	v_sub_f32_e32 v68, v68, v121
	v_pk_mul_f32 v[32:33], v[120:121], v[32:33] op_sel_hi:[0,1]
	v_pk_mul_f32 v[30:31], v[120:121], v[30:31] op_sel_hi:[0,1]
	v_pk_mul_f32 v[28:29], v[120:121], v[28:29] op_sel_hi:[0,1]
	v_pk_mul_f32 v[26:27], v[120:121], v[26:27] op_sel_hi:[0,1]
	v_pk_mul_f32 v[24:25], v[120:121], v[24:25] op_sel_hi:[0,1]
	v_pk_mul_f32 v[22:23], v[120:121], v[22:23] op_sel_hi:[0,1]
	v_pk_mul_f32 v[20:21], v[120:121], v[20:21] op_sel_hi:[0,1]
	v_pk_mul_f32 v[18:19], v[120:121], v[18:19] op_sel_hi:[0,1]
	v_pk_mul_f32 v[16:17], v[120:121], v[16:17] op_sel_hi:[0,1]
	v_pk_mul_f32 v[14:15], v[120:121], v[14:15] op_sel_hi:[0,1]
	v_pk_mul_f32 v[12:13], v[120:121], v[12:13] op_sel_hi:[0,1]
	v_pk_mul_f32 v[10:11], v[120:121], v[10:11] op_sel_hi:[0,1]
	v_pk_mul_f32 v[8:9], v[120:121], v[8:9] op_sel_hi:[0,1]
	v_pk_mul_f32 v[6:7], v[120:121], v[6:7] op_sel_hi:[0,1]
	v_pk_mul_f32 v[4:5], v[120:121], v[4:5] op_sel_hi:[0,1]
	v_pk_mul_f32 v[2:3], v[120:121], v[2:3] op_sel_hi:[0,1]
	v_sub_f32_e32 v69, v69, v121
	v_sub_f32_e32 v70, v70, v121
	v_sub_f32_e32 v71, v71, v121
	v_sub_f32_e32 v72, v72, v121
	v_sub_f32_e32 v73, v73, v121
	v_sub_f32_e32 v74, v74, v121
	v_sub_f32_e32 v75, v75, v121
	v_sub_f32_e32 v76, v76, v121
	v_sub_f32_e32 v77, v77, v121
	v_sub_f32_e32 v78, v78, v121
	v_sub_f32_e32 v79, v79, v121
	v_sub_f32_e32 v80, v80, v121
	v_sub_f32_e32 v81, v81, v121
	v_sub_f32_e32 v50, v50, v121
	v_sub_f32_e32 v51, v51, v121
	v_sub_f32_e32 v52, v52, v121
	v_sub_f32_e32 v53, v53, v121
	v_sub_f32_e32 v54, v54, v121
	v_sub_f32_e32 v55, v55, v121
	v_sub_f32_e32 v56, v56, v121
	v_sub_f32_e32 v57, v57, v121
	v_sub_f32_e32 v58, v58, v121
	v_sub_f32_e32 v59, v59, v121
	v_sub_f32_e32 v60, v60, v121
	v_sub_f32_e32 v61, v61, v121
	v_sub_f32_e32 v62, v62, v121
	v_sub_f32_e32 v63, v63, v121
	v_sub_f32_e32 v64, v64, v121
	v_sub_f32_e32 v65, v65, v121
	v_sub_f32_e32 v49, v49, v121
	v_sub_f32_e32 v48, v48, v121
	v_sub_f32_e32 v47, v47, v121
	v_sub_f32_e32 v46, v46, v121
	v_sub_f32_e32 v45, v45, v121
	v_sub_f32_e32 v44, v44, v121
	v_sub_f32_e32 v43, v43, v121
	v_sub_f32_e32 v42, v42, v121
	v_sub_f32_e32 v41, v41, v121
	v_sub_f32_e32 v40, v40, v121
	v_sub_f32_e32 v39, v39, v121
	v_sub_f32_e32 v38, v38, v121
	v_sub_f32_e32 v37, v37, v121
	v_sub_f32_e32 v36, v36, v121
	v_sub_f32_e32 v35, v35, v121
	v_sub_f32_e32 v34, v34, v121
	v_mul_f32_e32 v114, v114, v120
	s_branch .LBB3_6

	.amdhsa_kernel _Z11attn_kernelPKDF16_S0_S0_PDF16_P15HIP_vector_typeIfLj2EE
		.amdhsa_group_segment_fixed_size 49152
		.amdhsa_private_segment_fixed_size 0
		.amdhsa_kernarg_size 40
		.amdhsa_user_sgpr_count 2
		.amdhsa_user_sgpr_dispatch_ptr 0
		.amdhsa_user_sgpr_queue_ptr 0
		.amdhsa_user_sgpr_kernarg_segment_ptr 1
		.amdhsa_user_sgpr_dispatch_id 0
		.amdhsa_user_sgpr_kernarg_preload_length 0
		.amdhsa_user_sgpr_kernarg_preload_offset 0
		.amdhsa_user_sgpr_private_segment_size 0
		.amdhsa_uses_dynamic_stack 0
		.amdhsa_enable_private_segment 0
		.amdhsa_system_sgpr_workgroup_id_x 1
		.amdhsa_system_sgpr_workgroup_id_y 0
		.amdhsa_system_sgpr_workgroup_id_z 0
		.amdhsa_system_sgpr_workgroup_info 0
		.amdhsa_system_vgpr_workitem_id 0
		.amdhsa_next_free_vgpr 168
		.amdhsa_next_free_sgpr 96
		.amdhsa_accum_offset 168
		.amdhsa_reserve_vcc 1
		.amdhsa_float_round_mode_32 0
		.amdhsa_float_round_mode_16_64 0
		.amdhsa_float_denorm_mode_32 3
		.amdhsa_float_denorm_mode_16_64 3
		.amdhsa_dx10_clamp 1
		.amdhsa_ieee_mode 1
		.amdhsa_fp16_overflow 0
		.amdhsa_tg_split 0
		.amdhsa_exception_fp_ieee_invalid_op 0
		.amdhsa_exception_fp_denorm_src 0
		.amdhsa_exception_fp_ieee_div_zero 0
		.amdhsa_exception_fp_ieee_overflow 0
		.amdhsa_exception_fp_ieee_underflow 0
		.amdhsa_exception_fp_ieee_inexact 0
		.amdhsa_exception_int_div_zero 0
	.end_amdhsa_kernel

amdhsa.kernels:
  - .agpr_count:     0
    .args:
      - .actual_access:  read_only
        .address_space:  global
        .offset:         0
        .size:           8
        .value_kind:     global_buffer
      - .actual_access:  read_only
        .address_space:  global
        .offset:         8
        .size:           8
        .value_kind:     global_buffer
      - .actual_access:  read_only
        .address_space:  global
        .offset:         16
        .size:           8
        .value_kind:     global_buffer
      - .actual_access:  read_only
        .address_space:  global
        .offset:         24
        .size:           8
        .value_kind:     global_buffer
      - .actual_access:  read_only
        .address_space:  global
        .offset:         32
        .size:           8
        .value_kind:     global_buffer
      - .actual_access:  read_only
        .address_space:  global
        .offset:         40
        .size:           8
        .value_kind:     global_buffer
      - .actual_access:  read_only
        .address_space:  global
        .offset:         48
        .size:           8
        .value_kind:     global_buffer
      - .actual_access:  write_only
        .address_space:  global
        .offset:         56
        .size:           8
        .value_kind:     global_buffer
      - .actual_access:  write_only
        .address_space:  global
        .offset:         64
        .size:           8
        .value_kind:     global_buffer
    .group_segment_fixed_size: 0
    .kernarg_segment_align: 8
    .kernarg_segment_size: 72
    .language:       OpenCL C
    .language_version:
      - 2
      - 0
    .max_flat_workgroup_size: 256
    .name:           _Z11prep_kernelPKfS0_S0_S0_S0_S0_S0_PDF16_S1_
    .private_segment_fixed_size: 0
    .sgpr_count:     21
    .sgpr_spill_count: 0
    .symbol:         _Z11prep_kernelPKfS0_S0_S0_S0_S0_S0_PDF16_S1_.kd
    .uniform_work_group_size: 1
    .uses_dynamic_stack: false
    .vgpr_count:     10
    .vgpr_spill_count: 0
    .wavefront_size: 64
  - .agpr_count:     0
    .args:
      - .address_space:  global
        .offset:         0
        .size:           8
        .value_kind:     global_buffer
      - .address_space:  global
        .offset:         8
        .size:           8
        .value_kind:     global_buffer
      - .actual_access:  read_only
        .address_space:  global
        .offset:         16
        .size:           8
        .value_kind:     global_buffer
      - .actual_access:  read_only
        .address_space:  global
        .offset:         24
        .size:           8
        .value_kind:     global_buffer
      - .actual_access:  read_only
        .address_space:  global
        .offset:         32
        .size:           8
        .value_kind:     global_buffer
      - .actual_access:  write_only
        .address_space:  global
        .offset:         40
        .size:           8
        .value_kind:     global_buffer
      - .actual_access:  write_only
        .address_space:  global
        .offset:         48
        .size:           8
        .value_kind:     global_buffer
      - .actual_access:  write_only
        .address_space:  global
        .offset:         56
        .size:           8
        .value_kind:     global_buffer
    .group_segment_fixed_size: 30720
    .kernarg_segment_align: 8
    .kernarg_segment_size: 64
    .language:       OpenCL C
    .language_version:
      - 2
      - 0
    .max_flat_workgroup_size: 768
    .name:           _Z15qkv_proj_kernelPKDF16_S0_PKfS2_S2_PDF16_S3_S3_
    .private_segment_fixed_size: 0
    .sgpr_count:     47
    .sgpr_spill_count: 0
    .symbol:         _Z15qkv_proj_kernelPKDF16_S0_PKfS2_S2_PDF16_S3_S3_.kd
    .uniform_work_group_size: 1
    .uses_dynamic_stack: false
    .vgpr_count:     156
    .vgpr_spill_count: 0
    .wavefront_size: 64
  - .agpr_count:     0
    .args:
      - .address_space:  global
        .offset:         0
        .size:           8
        .value_kind:     global_buffer
      - .address_space:  global
        .offset:         8
        .size:           8
        .value_kind:     global_buffer
      - .actual_access:  read_only
        .address_space:  global
        .offset:         16
        .size:           8
        .value_kind:     global_buffer
      - .actual_access:  write_only
        .address_space:  global
        .offset:         24
        .size:           8
        .value_kind:     global_buffer
    .group_segment_fixed_size: 30720
    .kernarg_segment_align: 8
    .kernarg_segment_size: 32
    .language:       OpenCL C
    .language_version:
      - 2
      - 0
    .max_flat_workgroup_size: 384
    .name:           _Z15out_proj_kernelPKDF16_S0_PKfPf
    .private_segment_fixed_size: 0
    .sgpr_count:     67
    .sgpr_spill_count: 0
    .symbol:         _Z15out_proj_kernelPKDF16_S0_PKfPf.kd
    .uniform_work_group_size: 1
    .uses_dynamic_stack: false
    .vgpr_count:     144
    .vgpr_spill_count: 0
    .wavefront_size: 64
  - .agpr_count:     0
    .args:
      - .actual_access:  read_only
        .address_space:  global
        .offset:         0
        .size:           8
        .value_kind:     global_buffer
      - .address_space:  global
        .offset:         8
        .size:           8
        .value_kind:     global_buffer
      - .address_space:  global
        .offset:         16
        .size:           8
        .value_kind:     global_buffer
      - .actual_access:  write_only
        .address_space:  global
        .offset:         24
        .size:           8
        .value_kind:     global_buffer
      - .actual_access:  write_only
        .address_space:  global
        .offset:         32
        .size:           8
        .value_kind:     global_buffer
    .group_segment_fixed_size: 49152
    .kernarg_segment_align: 8
    .kernarg_segment_size: 40
    .language:       OpenCL C
    .language_version:
      - 2
      - 0
    .max_flat_workgroup_size: 256
    .name:           _Z11attn_kernelPKDF16_S0_S0_PDF16_P15HIP_vector_typeIfLj2EE
    .private_segment_fixed_size: 0
    .sgpr_count:     34
    .sgpr_spill_count: 0
    .symbol:         _Z11attn_kernelPKDF16_S0_S0_PDF16_P15HIP_vector_typeIfLj2EE.kd
    .uniform_work_group_size: 1
    .uses_dynamic_stack: false
    .vgpr_count:     168
    .vgpr_spill_count: 0
    .wavefront_size: 64
  - .agpr_count:     0
    .args:
      - .actual_access:  read_only
        .address_space:  global
        .offset:         0
        .size:           8
        .value_kind:     global_buffer
      - .actual_access:  read_only
        .address_space:  global
        .offset:         8
        .size:           8
        .value_kind:     global_buffer
      - .actual_access:  write_only
        .address_space:  global
        .offset:         16
        .size:           8
        .value_kind:     global_buffer
    .group_segment_fixed_size: 0
    .kernarg_segment_align: 8
    .kernarg_segment_size: 24
    .language:       OpenCL C
    .language_version:
      - 2
      - 0
    .max_flat_workgroup_size: 256
    .name:           _Z14combine_kernelPKDF16_PK15HIP_vector_typeIfLj2EEPDF16_
    .private_segment_fixed_size: 0
    .sgpr_count:     16
    .sgpr_spill_count: 0
    .symbol:         _Z14combine_kernelPKDF16_PK15HIP_vector_typeIfLj2EEPDF16_.kd
    .uniform_work_group_size: 1
    .uses_dynamic_stack: false
    .vgpr_count:     44
    .vgpr_spill_count: 0
    .wavefront_size: 64
